# LN phases: wave-major row assignment (row = wave*gridDim + block) so every workgroup gets 66 rows instead of 64 or 72
# speedup vs baseline: 1.0244x; 1.0054x over previous
.LBB0_502:
	s_andn2_b64 vcc, exec, s[0:1]
	s_cbranch_vccnz .LBB0_595
	s_waitcnt vmcnt(0)
	v_mov_b32_e32 v8, v0
	s_nop 0
	v_readfirstlane_b32 s0, v8
	s_ashr_i32 s50, s0, 6
	s_mul_i32 s0, s50, s33
	s_add_i32 s52, s0, s2
	s_nop 0
	s_mov_b64 s[0:1], s[96:97]
	s_load_dwordx2 s[4:5], s[0:1], 0xa8
	v_and_b32_e32 v68, 63, v8
	s_cmp_lt_i32 s52, s26
	s_cselect_b64 s[42:43], -1, 0
	s_cmp_ge_i32 s52, s26
	v_lshlrev_b32_e32 v144, 3, v68
	v_lshlrev_b32_e32 v2, 4, v68
	s_cbranch_scc1 .LBB0_512
	s_ashr_i32 s53, s52, 31
	s_lshl_b64 s[8:9], s[52:53], 11
	s_waitcnt lgkmcnt(0)
	s_add_u32 s8, s4, s8
	s_addc_u32 s9, s5, s9
	v_mov_b32_e32 v145, v3
	v_lshl_add_u64 v[6:7], s[8:9], 0, v[144:145]
	v_add_co_u32_e32 v4, vcc, 0x17600000, v6
	s_cmp_lg_u32 s36, 0
	s_nop 0
	v_addc_co_u32_e32 v5, vcc, 0, v7, vcc
	global_load_dwordx2 v[170:171], v[4:5], off
	s_cselect_b64 s[8:9], -1, 0
	s_lshl_b64 s[40:41], s[52:53], 12
	s_add_u32 s40, s4, s40
	s_addc_u32 s41, s5, s41
	v_lshl_add_u64 v[4:5], s[40:41], 0, v[2:3]
	s_mov_b64 s[40:41], 0xb000000
	s_cmp_eq_u32 s36, 0
	v_lshl_add_u64 v[4:5], v[4:5], 0, s[40:41]
	s_cbranch_scc1 .LBB0_506
	global_load_dwordx4 v[96:99], v[4:5], off

.LBB0_513:
	s_mul_i32 s27, s9, 0xab
	s_bfe_u32 s27, s27, 0x70009
	s_mul_i32 s27, s27, 3
	s_sub_i32 s27, s9, s27
	s_and_b32 s27, s27, 0xff
	s_mul_i32 s37, s36, 3
	s_add_i32 s27, s27, s37
	s_cmp_lt_u32 s9, 6
	s_mul_hi_u32 s37, s27, 0xc000
	s_mul_i32 s27, s27, 0xc000
	s_cselect_b32 s40, 0x2000, s77
	s_add_u32 s27, s6, s27
	s_addc_u32 s37, s8, s37
	s_cmp_gt_u32 s9, 2
	s_cselect_b32 s40, s40, 0x1800
	s_lshl_b32 s40, s40, 2
	s_add_u32 s40, s27, s40
	s_addc_u32 s41, s37, 0
	v_lshl_add_u64 v[8:9], v[4:5], 2, s[40:41]
	global_load_dwordx4 v[8:11], v[8:9], off
	s_add_i32 s9, s9, 1
	s_cmp_eq_u32 s9, 9
	s_waitcnt vmcnt(0)
	ds_write_b128 v6, v[8:11]
	v_add_u32_e32 v6, 0x2000, v6
	s_cbranch_scc0 .LBB0_513
	s_andn2_b64 vcc, exec, s[42:43]
	s_waitcnt lgkmcnt(0)
	s_barrier
	s_cbranch_vccnz .LBB0_545
	v_add_u32_e32 v145, 0, v2
	ds_read_b128 v[4:7], v145
	ds_read_b128 v[8:11], v145 offset:1024
	ds_read_b128 v[12:15], v145 offset:8192
	ds_read_b128 v[16:19], v145 offset:9216
	ds_read_b128 v[20:23], v145 offset:2048
	ds_read_b128 v[24:27], v145 offset:3072
	ds_read_b128 v[28:31], v145 offset:10240
	ds_read_b128 v[32:35], v145 offset:11264
	ds_read_b128 v[36:39], v145 offset:4096
	ds_read_b128 v[40:43], v145 offset:5120
	ds_read_b128 v[44:47], v145 offset:12288
	ds_read_b128 v[48:51], v145 offset:13312
	ds_read_b128 v[52:55], v145 offset:6144
	ds_read_b128 v[56:59], v145 offset:7168
	ds_read_b128 v[60:63], v145 offset:14336
	ds_read_b128 v[64:67], v145 offset:15360
	s_cmp_lg_u32 s36, 0
	s_cselect_b64 s[44:45], -1, 0
	s_add_u32 s27, s0, 16
	s_addc_u32 s37, s1, 0
	s_ashr_i32 s53, s52, 31
	s_lshl_b64 s[8:9], s[52:53], 2
	s_add_u32 s56, s8, 0x3d200000
	s_addc_u32 s57, s9, 0
	s_lshl_b64 s[8:9], s[52:53], 11
	v_or_b32_e32 v146, s8, v144
	v_mov_b32_e32 v147, s9
	v_lshl_or_b32 v148, v68, 2, s8
	v_mov_b32_e32 v149, s9
	s_lshl_b64 s[8:9], s[52:53], 12
	v_readlane_b32 s6, v253, 11
	v_or_b32_e32 v150, s8, v2
	s_add_i32 s8, s52, s84
	v_mov_b32_e32 v151, s9
	s_ashr_i32 s9, s8, 31
	s_lshl_b64 s[42:43], s[8:9], 12
	s_lshl_b64 s[8:9], s[8:9], 11
	v_cmp_eq_u32_e64 s[40:41], 0, v68
	s_lshl_b64 s[46:47], s[52:53], 13
	v_or_b32_e32 v152, s42, v2
	v_mov_b32_e32 v153, s43
	v_or_b32_e32 v154, s8, v144
	v_mov_b32_e32 v155, s9
	s_and_b64 vcc, exec, s[44:45]
	s_cbranch_vccnz .Lln0_pre_done
	v_lshlrev_b32_e32 v228, 2, v144
	s_add_i32 s6, s52, 0xffffc000
	s_lshl_b64 s[42:43], s[6:7], 13
	s_cmpk_lt_i32 s52, 0x4000
	s_cselect_b32 s9, s1, s37
	s_cselect_b32 s8, s0, s27
	s_cselect_b32 s100, s46, s42
	s_cselect_b32 s101, s47, s43
	s_load_dwordx2 s[8:9], s[8:9], 0x0
	s_waitcnt lgkmcnt(0)
	s_add_u32 s8, s8, s100
	s_addc_u32 s9, s9, s101
	global_load_dwordx4 v[182:185], v228, s[8:9] offset:16
	global_load_dwordx4 v[186:189], v228, s[8:9]
	global_load_dwordx4 v[190:193], v228, s[8:9] offset:2064
	global_load_dwordx4 v[194:197], v228, s[8:9] offset:2048
	s_add_u32 s8, s8, 0x1000
	s_addc_u32 s9, s9, 0
	global_load_dwordx4 v[198:201], v228, s[8:9]
	global_load_dwordx4 v[202:205], v228, s[8:9] offset:16
	global_load_dwordx4 v[220:223], v228, s[8:9] offset:2048
	global_load_dwordx4 v[224:227], v228, s[8:9] offset:2064
